# attention loop LDS-DMA issue: m0 written directly by the address add, the pointer VALU op placed in the mandatory wait slot (nine scalar instructions fewer per iteration)
# baseline (speedup 1.0000x reference)
.LBB0_1319:
	v_mfma_f32_32x32x16_bf16 v[82:97], v[138:141], v[98:101], 0
	s_add_i32 s45, s44, -2
	s_mul_hi_i32 s50, s45, 0x55555556
	s_mul_i32 s50, s50, 3
	s_sub_i32 s45, s45, s50
	v_lshl_add_u32 v162, s45, 13, v240
	ds_read_b64_tr_b16 v[142:143], v162 offset:40960
	ds_read_b64_tr_b16 v[144:145], v162 offset:41472
	s_add_i32 s45, s44, -1
	v_add_f32_e32 v66, v50, v51
	v_add_f32_e32 v67, v52, v53
	v_add_f32_e32 v66, v66, v67
	v_cvt_pk_bf16_f32 v138, v50, v51
	v_cvt_pk_bf16_f32 v139, v52, v53
	ds_read_b64_tr_b16 v[146:147], v162 offset:45056
	ds_read_b64_tr_b16 v[148:149], v162 offset:45568
	v_add_f32_e32 v50, v54, v55
	v_add_f32_e32 v51, v56, v57
	v_add_f32_e32 v50, v50, v51
	v_add_f32_e32 v50, v50, v66
	v_mfma_f32_32x32x16_bf16 v[66:81], v[130:133], v[98:101], 0
	v_cvt_pk_bf16_f32 v140, v54, v55
	v_cvt_pk_bf16_f32 v141, v56, v57
	s_and_b32 s50, s45, 3
	s_mulk_i32 s50, 0x2800
	v_add_u32_e32 v150, s50, v238
	ds_read_b128 v[130:133], v150 offset:6144
	ds_read_b128 v[158:161], v150 offset:6656
	ds_read_b64_tr_b16 v[54:55], v162 offset:41984
	ds_read_b64_tr_b16 v[56:57], v162 offset:42496
	v_mfma_f32_32x32x16_bf16 v[82:97], v[134:137], v[102:105], v[82:97]
	v_add_f32_e32 v51, v58, v59
	v_add_f32_e32 v52, v60, v61
	v_add_f32_e32 v51, v51, v52
	v_add_f32_e32 v52, v51, v50
	v_cvt_pk_bf16_f32 v50, v58, v59
	v_cvt_pk_bf16_f32 v51, v60, v61
	ds_read_b64_tr_b16 v[58:59], v162 offset:46080
	ds_read_b64_tr_b16 v[60:61], v162 offset:46592
	v_mfma_f32_32x32x16_bf16 v[66:81], v[126:129], v[102:105], v[66:81]
	v_add_f32_e32 v53, v62, v63
	v_add_f32_e32 v126, v64, v65
	v_add_f32_e32 v53, v53, v126
	v_add_f32_e32 v151, v53, v52
	v_cvt_pk_bf16_f32 v52, v62, v63
	v_cvt_pk_bf16_f32 v53, v64, v65
	ds_read_b128 v[126:129], v150 offset:8192
	ds_read_b128 v[134:137], v150 offset:8704
	ds_read_b64_tr_b16 v[62:63], v162 offset:43008
	ds_read_b64_tr_b16 v[64:65], v162 offset:43520
	v_mfma_f32_32x32x16_bf16 v[82:97], v[122:125], v[106:109], v[82:97]
	v_add_f32_e32 v122, v34, v35
	v_add_f32_e32 v123, v36, v37
	v_add_f32_e32 v122, v122, v123
	v_add_f32_e32 v122, v122, v151
	v_cvt_pk_bf16_f32 v34, v34, v35
	v_cvt_pk_bf16_f32 v35, v36, v37
	ds_read_b64_tr_b16 v[150:151], v162 offset:47104
	ds_read_b64_tr_b16 v[152:153], v162 offset:47616
	v_mfma_f32_32x32x16_bf16 v[66:81], v[118:121], v[106:109], v[66:81]
	v_add_f32_e32 v36, v38, v39
	v_add_f32_e32 v37, v40, v41
	v_add_f32_e32 v36, v36, v37
	v_add_f32_e32 v118, v36, v122
	v_cvt_pk_bf16_f32 v36, v38, v39
	v_cvt_pk_bf16_f32 v37, v40, v41
	ds_read_b64_tr_b16 v[154:155], v162 offset:44032
	ds_read_b64_tr_b16 v[156:157], v162 offset:44544
	s_waitcnt lgkmcnt(13)
	v_mfma_f32_32x32x16_bf16 v[82:97], v[130:133], v[110:113], v[82:97]
	v_add_f32_e32 v38, v42, v43
	v_add_f32_e32 v39, v44, v45
	v_add_f32_e32 v38, v38, v39
	v_add_f32_e32 v40, v38, v118
	v_cvt_pk_bf16_f32 v38, v42, v43
	v_cvt_pk_bf16_f32 v39, v44, v45
	ds_read_b64_tr_b16 v[42:43], v162 offset:48128
	ds_read_b64_tr_b16 v[44:45], v162 offset:48640
	s_waitcnt lgkmcnt(14)
	v_mfma_f32_32x32x16_bf16 v[66:81], v[158:161], v[110:113], v[66:81]
	v_add_f32_e32 v41, v46, v47
	v_add_f32_e32 v118, v48, v49
	v_add_f32_e32 v41, v41, v118
	v_add_f32_e32 v166, v41, v40
	v_cvt_pk_bf16_f32 v40, v46, v47
	v_cvt_pk_bf16_f32 v41, v48, v49
	s_waitcnt lgkmcnt(9)
	v_mfma_f32_32x32x16_bf16 v[82:97], v[126:129], v[114:117], v[82:97]
	s_waitcnt lgkmcnt(8)
	v_mfma_f32_32x32x16_bf16 v[66:81], v[134:137], v[114:117], v[66:81]
	s_add_i32 s61, s44, 2
	s_cmp_lt_i32 s61, s71
	s_cselect_b64 s[52:53], -1, 0
	s_cmp_ge_i32 s61, s71
	s_cselect_b64 s[50:51], -1, 0
	s_cbranch_scc1 .LBB0_1322
	s_and_b32 s54, s61, 3
	s_mulk_i32 s54, 0x2800
	s_add_i32 m0, s54, s66
	s_nop 0
	global_load_lds_dwordx4 v[222:223], off
	s_and_b64 vcc, exec, s[42:43]
	s_cbranch_vccnz .LBB0_1322
	s_add_i32 m0, s54, s70
	s_nop 0
	global_load_lds_dwordx4 v[220:221], off
.LBB0_1322:
	s_mul_hi_i32 s54, s44, 0x55555556
	s_mul_i32 s54, s54, 3
	s_sub_i32 s54, s44, s54
	s_lshl_b32 s54, s54, 13
	s_add_i32 m0, s54, s72
	s_nop 0
	global_load_lds_dwordx4 v[218:219], off
	s_cmp_lt_i32 s45, s68
	s_cbranch_scc1 .LBB0_1324
	v_add_u32_e32 v47, 0xffffffa5, v195
	v_add_u32_e32 v46, 0xffffff85, v195
	v_cmp_le_i32_e32 vcc, v47, v191
	s_nop 1
	v_cndmask_b32_e32 v66, v230, v66, vcc
	v_cmp_lt_i32_e32 vcc, v46, v191
	s_nop 1
	v_cndmask_b32_e32 v83, v230, v83, vcc
	v_cmp_le_i32_e32 vcc, v46, v191
	v_add_u32_e32 v46, 0xffffffa6, v195
	s_nop 0
	v_cndmask_b32_e32 v82, v230, v82, vcc
	v_cmp_le_i32_e32 vcc, v46, v191
	v_add_u32_e32 v46, 0xffffff87, v195
	s_nop 0
	v_cndmask_b32_e32 v67, v230, v67, vcc
	v_cmp_le_i32_e32 vcc, v46, v191
	v_add_u32_e32 v46, 0xffffffa7, v195
	s_nop 0
	v_cndmask_b32_e32 v84, v230, v84, vcc
	v_cmp_le_i32_e32 vcc, v46, v191
	v_add_u32_e32 v46, 0xffffff88, v195
	s_nop 0
	v_cndmask_b32_e32 v68, v230, v68, vcc
	v_cmp_le_i32_e32 vcc, v46, v191
	v_add_u32_e32 v46, 0xffffffa8, v195
	s_nop 0
	v_cndmask_b32_e32 v85, v230, v85, vcc
	v_cmp_le_i32_e32 vcc, v46, v191
	v_add_u32_e32 v46, 0xffffff8d, v195
	s_nop 0
	v_cndmask_b32_e32 v69, v230, v69, vcc
	v_cmp_le_i32_e32 vcc, v46, v191
	v_add_u32_e32 v46, 0xffffffad, v195
	s_nop 0
	v_cndmask_b32_e32 v86, v230, v86, vcc
	v_cmp_le_i32_e32 vcc, v46, v191
	v_add_u32_e32 v46, 0xffffff8e, v195
	s_nop 0
	v_cndmask_b32_e32 v70, v230, v70, vcc
	v_cmp_le_i32_e32 vcc, v46, v191
	v_add_u32_e32 v46, 0xffffffae, v195
	s_nop 0
	v_cndmask_b32_e32 v87, v230, v87, vcc
	v_cmp_le_i32_e32 vcc, v46, v191
	v_add_u32_e32 v46, 0xffffff8f, v195
	s_nop 0
	v_cndmask_b32_e32 v71, v230, v71, vcc
	v_cmp_le_i32_e32 vcc, v46, v191
	v_add_u32_e32 v46, 0xffffffaf, v195
	s_nop 0
	v_cndmask_b32_e32 v88, v230, v88, vcc
	v_cmp_le_i32_e32 vcc, v46, v191
	v_add_u32_e32 v46, 0xffffff90, v195
	s_nop 0
	v_cndmask_b32_e32 v72, v230, v72, vcc
	v_cmp_le_i32_e32 vcc, v46, v191
	v_add_u32_e32 v46, 0xffffffb0, v195
	s_nop 0
	v_cndmask_b32_e32 v89, v230, v89, vcc
	v_cmp_le_i32_e32 vcc, v46, v191
	v_add_u32_e32 v46, 0xffffff95, v195
	s_nop 0
	v_cndmask_b32_e32 v73, v230, v73, vcc
	v_cmp_le_i32_e32 vcc, v46, v191
	v_add_u32_e32 v46, 0xffffffb5, v195
	s_nop 0
	v_cndmask_b32_e32 v90, v230, v90, vcc
	v_cmp_le_i32_e32 vcc, v46, v191
	v_add_u32_e32 v46, 0xffffff96, v195
	s_nop 0
	v_cndmask_b32_e32 v74, v230, v74, vcc
	v_cmp_le_i32_e32 vcc, v46, v191
	v_add_u32_e32 v46, 0xffffffb6, v195
	s_nop 0
	v_cndmask_b32_e32 v91, v230, v91, vcc
	v_cmp_le_i32_e32 vcc, v46, v191
	v_add_u32_e32 v46, 0xffffff97, v195
	s_nop 0
	v_cndmask_b32_e32 v75, v230, v75, vcc
	v_cmp_le_i32_e32 vcc, v46, v191
	v_add_u32_e32 v46, 0xffffffb7, v195
	s_nop 0
	v_cndmask_b32_e32 v92, v230, v92, vcc
	v_cmp_le_i32_e32 vcc, v46, v191
	v_add_u32_e32 v46, 0xffffff98, v195
	s_nop 0
	v_cndmask_b32_e32 v76, v230, v76, vcc
	v_cmp_le_i32_e32 vcc, v46, v191
	v_add_u32_e32 v46, 0xffffffb8, v195
	s_nop 0
	v_cndmask_b32_e32 v93, v230, v93, vcc
	v_cmp_le_i32_e32 vcc, v46, v191
	v_add_u32_e32 v46, 0xffffff9d, v195
	s_nop 0
	v_cndmask_b32_e32 v77, v230, v77, vcc
	v_cmp_le_i32_e32 vcc, v46, v191
	v_add_u32_e32 v46, 0xffffffbd, v195
	s_nop 0
	v_cndmask_b32_e32 v94, v230, v94, vcc
	v_cmp_le_i32_e32 vcc, v46, v191
	v_add_u32_e32 v46, 0xffffff9e, v195
	s_nop 0
	v_cndmask_b32_e32 v78, v230, v78, vcc
	v_cmp_le_i32_e32 vcc, v46, v191
	v_add_u32_e32 v46, 0xffffffbe, v195
	s_nop 0
	v_cndmask_b32_e32 v95, v230, v95, vcc
	v_cmp_le_i32_e32 vcc, v46, v191
	v_add_u32_e32 v46, 0xffffff9f, v195
	s_nop 0
	v_cndmask_b32_e32 v79, v230, v79, vcc
	v_cmp_le_i32_e32 vcc, v46, v191
	v_add_u32_e32 v46, 0xffffffbf, v195
	s_nop 0
	v_cndmask_b32_e32 v96, v230, v96, vcc
	v_cmp_le_i32_e32 vcc, v46, v191
	v_add_u32_e32 v46, 0xffffffa0, v195
	s_nop 0
	v_cndmask_b32_e32 v80, v230, v80, vcc
	v_cmp_le_i32_e32 vcc, v46, v191
	v_subrev_u32_e32 v46, 64, v195
	s_nop 0
	v_cndmask_b32_e32 v97, v230, v97, vcc
	v_cmp_le_i32_e32 vcc, v46, v191
	s_nop 1
	v_cndmask_b32_e32 v81, v230, v81, vcc

.LBB0_1331:
	v_mfma_f32_32x32x16_bf16 v[50:65], v[138:141], v[98:101], 0
	s_mul_hi_i32 s52, s45, 0x55555556
	s_mul_i32 s52, s52, 3
	s_sub_i32 s45, s45, s52
	v_lshl_add_u32 v199, s45, 13, v240
	ds_read_b64_tr_b16 v[162:163], v199 offset:40960
	ds_read_b64_tr_b16 v[164:165], v199 offset:41472
	s_waitcnt lgkmcnt(7)
	v_add_f32_e32 v34, v82, v83
	v_add_f32_e32 v35, v84, v85
	v_add_f32_e32 v34, v34, v35
	v_cvt_pk_bf16_f32 v154, v82, v83
	v_cvt_pk_bf16_f32 v155, v84, v85
	ds_read_b64_tr_b16 v[158:159], v199 offset:45056
	ds_read_b64_tr_b16 v[160:161], v199 offset:45568
	v_add_f32_e32 v35, v86, v87
	v_add_f32_e32 v36, v88, v89
	v_add_f32_e32 v35, v35, v36
	v_add_f32_e32 v82, v35, v34
	s_waitcnt lgkmcnt(8)
	v_mfma_f32_32x32x16_bf16 v[34:49], v[130:133], v[98:101], 0
	v_cvt_pk_bf16_f32 v156, v86, v87
	v_cvt_pk_bf16_f32 v157, v88, v89
	ds_read_b128 v[170:173], v197 offset:6144
	ds_read_b128 v[174:177], v197 offset:6656
	ds_read_b64_tr_b16 v[150:151], v199 offset:41984
	ds_read_b64_tr_b16 v[152:153], v199 offset:42496
	s_waitcnt lgkmcnt(11)
	v_mfma_f32_32x32x16_bf16 v[50:65], v[134:137], v[102:105], v[50:65]
	v_add_f32_e32 v83, v90, v91
	v_add_f32_e32 v84, v92, v93
	v_add_f32_e32 v83, v83, v84
	v_add_f32_e32 v82, v83, v82
	v_cvt_pk_bf16_f32 v142, v90, v91
	v_cvt_pk_bf16_f32 v143, v92, v93
	ds_read_b64_tr_b16 v[146:147], v199 offset:46080
	ds_read_b64_tr_b16 v[148:149], v199 offset:46592
	s_waitcnt lgkmcnt(12)
	v_mfma_f32_32x32x16_bf16 v[34:49], v[126:129], v[102:105], v[34:49]
	v_add_f32_e32 v83, v94, v95
	v_add_f32_e32 v84, v96, v97
	v_add_f32_e32 v83, v83, v84
	v_add_f32_e32 v82, v83, v82
	v_cvt_pk_bf16_f32 v144, v94, v95
	v_cvt_pk_bf16_f32 v145, v96, v97
	ds_read_b128 v[248:251], v197 offset:8192
	ds_read_b128 v[232:235], v197 offset:8704
	ds_read_b64_tr_b16 v[90:91], v199 offset:43008
	ds_read_b64_tr_b16 v[92:93], v199 offset:43520
	s_waitcnt lgkmcnt(14)
	v_mfma_f32_32x32x16_bf16 v[50:65], v[122:125], v[106:109], v[50:65]
	v_add_f32_e32 v83, v66, v67
	v_add_f32_e32 v84, v68, v69
	v_add_f32_e32 v83, v83, v84
	v_add_f32_e32 v84, v83, v82
	v_cvt_pk_bf16_f32 v82, v66, v67
	v_cvt_pk_bf16_f32 v83, v68, v69
	ds_read_b64_tr_b16 v[86:87], v199 offset:47104
	ds_read_b64_tr_b16 v[88:89], v199 offset:47616
	v_mfma_f32_32x32x16_bf16 v[34:49], v[118:121], v[106:109], v[34:49]
	v_add_f32_e32 v66, v70, v71
	v_add_f32_e32 v67, v72, v73
	v_add_f32_e32 v66, v66, v67
	v_add_f32_e32 v66, v66, v84
	v_cvt_pk_bf16_f32 v84, v70, v71
	v_cvt_pk_bf16_f32 v85, v72, v73
	ds_read_b64_tr_b16 v[70:71], v199 offset:44032
	ds_read_b64_tr_b16 v[72:73], v199 offset:44544
	s_waitcnt lgkmcnt(13)
	v_mfma_f32_32x32x16_bf16 v[50:65], v[170:173], v[110:113], v[50:65]
	v_add_f32_e32 v67, v74, v75
	v_add_f32_e32 v68, v76, v77
	v_add_f32_e32 v67, v67, v68
	v_add_f32_e32 v68, v67, v66
	v_cvt_pk_bf16_f32 v66, v74, v75
	v_cvt_pk_bf16_f32 v67, v76, v77
	ds_read_b64_tr_b16 v[74:75], v199 offset:48128
	ds_read_b64_tr_b16 v[76:77], v199 offset:48640
	s_waitcnt lgkmcnt(14)
	v_mfma_f32_32x32x16_bf16 v[34:49], v[174:177], v[110:113], v[34:49]
	v_add_f32_e32 v69, v78, v79
	v_add_f32_e32 v94, v80, v81
	v_add_f32_e32 v69, v69, v94
	v_add_f32_e32 v94, v69, v68
	v_cvt_pk_bf16_f32 v68, v78, v79
	v_cvt_pk_bf16_f32 v69, v80, v81
	s_waitcnt lgkmcnt(9)
	v_mfma_f32_32x32x16_bf16 v[50:65], v[248:251], v[114:117], v[50:65]
	s_waitcnt lgkmcnt(8)
	v_mfma_f32_32x32x16_bf16 v[34:49], v[232:235], v[114:117], v[34:49]
	s_add_i32 s54, s44, 3
	s_cmp_lt_i32 s54, s71
	s_cselect_b64 s[52:53], -1, 0
	s_cbranch_scc0 .LBB0_1334
	s_ashr_i32 s55, s54, 31
	s_and_b32 s45, s54, 3
	s_lshl_b64 s[58:59], s[54:55], 17
	s_mulk_i32 s45, 0x2800
	s_add_i32 m0, s45, s66
	v_lshl_add_u64 v[78:79], v[212:213], 0, s[58:59]
	global_load_lds_dwordx4 v[78:79], off
	s_and_b64 vcc, exec, s[42:43]
	s_cbranch_vccnz .LBB0_1334
	s_lshl_b64 s[54:55], s[54:55], 11
	s_add_i32 m0, s45, s70
	v_lshl_add_u64 v[78:79], v[214:215], 0, s[54:55]
	global_load_lds_dwordx4 v[78:79], off
.LBB0_1334:
	s_add_i32 s54, s44, 1
	s_cmp_lt_i32 s54, s71
	s_cselect_b64 s[58:59], -1, 0
	s_cbranch_scc0 .LBB0_1336
	s_mul_hi_i32 s45, s54, 0x55555556
	s_mul_i32 s45, s45, 3
	s_sub_i32 s45, s54, s45
	s_ashr_i32 s55, s54, 31
	s_lshl_b64 s[62:63], s[54:55], 17
	s_lshl_b32 s45, s45, 13
	s_add_i32 m0, s45, s72
	v_lshl_add_u64 v[78:79], v[216:217], 0, s[62:63]
	global_load_lds_dwordx4 v[78:79], off
